# phase B rows: all rows of a wave prefetched up front into register sets (on v11)
# speedup vs baseline: 1.0002x; 1.0002x over previous
; #define LAS __attribute__((address_space(3)))
; __device__ __forceinline__ int opaque_tid() { int t = threadIdx.x; asm volatile("" : "+v"(t)); return t; }
; __device__ __forceinline__ unsigned char* opaque_ptr(unsigned char* q) { long z = 0; asm volatile("" : "+s"(z)); return q + z; }
; template <bool MAIN, bool CONV>
; __device__ __forceinline__ void b_row(const Params& p, unsigned char* ws, int l, int row, int lane) {
;     ...
;     if (MAIN) {
;         if (lane < 48) vq = *(const u32x4*)(pr + C_CQ + lane * 8);
;         vkv = *(const u32x2*)(pr + C_CKV + lane * 4);
;         vkr = pr[C_KR + lane];
;         vs5 = *(const u32x4*)(pr + C_S5 + lane * 8);
;         if (lane < 48) { const float* g = p.in[I_QNG] + l * 384 + lane * 8; gq0 = *(const f32x4*)g; gq1 = *(const f32x4*)(g + 4); }
;         gkv = *(const f32x4*)(p.in[I_KVNG] + l * 256 + lane * 4);
;         if (lat) { const int pos = lane >= 32 ? (t & 63) : (t >> 6); rope = ((const f32x2*)(ws + WS_ROPE))[pos * 16 + (lane & 15)]; }
; __device__ __forceinline__ void ph_rowsplit(const Params& p, int l, LAS unsigned char* lds) {
;     const int tid = opaque_tid(), lane = tid & 63, wave = tid >> 6;
;     unsigned char* ws = opaque_ptr(p.ws);
;     const bf16_t* P = (const bf16_t*)(ws + WS_PA);
;     bf16_t* CAT = (bf16_t*)(ws + WS_CAT);
;     const int nsgu = gridDim.x == 256 ? 0 : ((l == 0) ? B_SGU : 256);
;     const int G_ = (int)gridDim.x, c_ = (int)blockIdx.x, nx = nsgu > G_ ? nsgu - G_ : 0;
;     const bool bal = nx > 0 && nx < G_ && nsgu <= 2 * G_;
;     const int nfew = bal ? 2 * nx : 0;
;     const int nmine = (c_ < nsgu ? 1 : 0) + (c_ < nx ? 1 : 0);
;     int rit = bal ? (c_ < nx ? c_ : nfew + (c_ - nx)) : c_; const int rstride = bal ? (c_ < nx ? nx : G_ - nx) : G_; const int rend = bal ? (c_ < nx ? nfew : B_ROWITEMS) : B_ROWITEMS;
;     for (int k = 0; ; ++k) {
;         int it;
;         if (k < nmine) it = B_ROWITEMS + c_ + k * G_;
;         else { if (rit >= rend) break; it = rit; rit += rstride; }
;         if (it < B_ROWITEMS) {
;             const int row = it * 8 + wave;
;             if (gridDim.x == 256) b_row<true, false>(p, ws, l, row, lane); else b_row<true, true>(p, ws, l, row, lane);
.LBB0_465:
	s_andn2_b64 vcc, exec, s[0:1]
	v_readlane_b32 s0, v252, 5
	v_readlane_b32 s1, v252, 6
	s_mov_b32 s1, s5
	v_writelane_b32 v252, s0, 5
	s_nop 1
	v_writelane_b32 v252, s1, 6
	s_cbranch_vccnz .LBB0_590
	v_readlane_b32 s0, v252, 20
	v_readlane_b32 s1, v252, 21
	s_and_b64 s[0:1], s[0:1], exec
	s_movk_i32 s0, 0x120
	s_cselect_b32 s2, s0, 0x100
	v_readlane_b32 s0, v251, 50
	v_readlane_b32 s1, v251, 51
	s_and_b64 s[0:1], s[0:1], exec
	s_cselect_b32 s4, 0, s2
	s_sub_i32 s0, s4, s94
	s_cmp_gt_i32 s4, s94
	s_cselect_b32 s13, s0, 0
	s_cmp_lt_i32 s13, 1
	s_cselect_b64 s[0:1], -1, 0
	s_cmp_le_i32 s94, s13
	s_cselect_b64 s[2:3], -1, 0
	s_or_b64 s[0:1], s[0:1], s[2:3]
	v_readlane_b32 s2, v253, 18
	s_cmp_gt_u32 s4, s2
	s_cselect_b64 s[2:3], -1, 0
	s_or_b64 s[0:1], s[0:1], s[2:3]
	s_lshl_b32 s14, s13, 1
	s_and_b64 s[2:3], s[0:1], exec
	s_cselect_b32 s14, 0, s14
	s_cmp_lt_i32 s92, s13
	s_cselect_b64 s[2:3], -1, 0
	s_and_b64 s[2:3], s[2:3], exec
	s_cselect_b32 s15, s14, 0x480
	s_sub_i32 s16, s94, s13
	s_cmp_lt_i32 s92, s13
	s_cselect_b64 vcc, -1, 0
	s_and_b64 s[2:3], vcc, exec
	s_cselect_b32 s16, s13, s16
	s_cmp_lt_i32 s92, s4
	s_cselect_b64 s[2:3], -1, 0
	s_waitcnt vmcnt(0)
	v_cndmask_b32_e64 v2, 0, 1, s[2:3]
	v_addc_co_u32_e64 v75, s[2:3], 0, v2, vcc
	s_sub_i32 s4, s92, s13
	s_or_b64 s[2:3], vcc, s[0:1]
	s_add_i32 s4, s4, s14
	s_and_b64 s[2:3], s[2:3], exec
	s_cselect_b32 s31, s92, s4
	s_and_b64 s[0:1], s[0:1], exec
	v_readlane_b32 s2, v252, 5
	s_cselect_b32 s13, s94, s16
	s_cselect_b32 s24, 0x480, s15
	s_lshl_b32 s18, s2, 9
	s_mov_b32 s19, s5
	v_readlane_b32 s52, v251, 16
	s_lshl_b32 s0, s2, 8
	s_lshl_b64 s[14:15], s[18:19], 2
	v_readlane_b32 s56, v251, 20
	s_mul_i32 s4, s2, 0x180
	v_readlane_b32 s57, v251, 21
	s_add_u32 s25, s56, s14
	v_readlane_b32 s62, v251, 26
	s_addc_u32 s26, s57, s15
	s_lshl_b64 s[14:15], s[4:5], 2
	s_mov_b32 s1, s5
	v_readlane_b32 s63, v251, 27
	s_add_u32 s14, s62, s14
	v_readlane_b32 s3, v252, 6
	v_readlane_b32 s66, v251, 30
	s_addc_u32 s15, s63, s15
	s_lshl_b64 s[0:1], s[0:1], 2
	s_mulk_i32 s2, 0x600
	s_mov_b32 s3, s5
	v_readlane_b32 s67, v251, 31
	s_add_u32 s0, s66, s0
	v_readlane_b32 s36, v251, 32
	s_addc_u32 s1, s67, s1
	s_lshl_b64 s[2:3], s[2:3], 2
	v_readlane_b32 s42, v251, 38
	v_readlane_b32 s43, v251, 39
	s_add_u32 s2, s42, s2
	s_addc_u32 s3, s43, s3
	v_mov_b32_e32 v4, v0
	s_mov_b64 s[16:17], 0
	s_add_u32 s20, s84, s16
	v_and_b32_e32 v74, 63, v4
	s_addc_u32 s21, s85, s17
	v_lshlrev_b32_e32 v76, 3, v74
	v_mov_b32_e32 v77, v207
	s_add_u32 s22, s20, 0x1f1b8000
	v_lshl_add_u64 v[2:3], s[20:21], 0, v[76:77]
	s_mov_b64 s[16:17], 0x2fc78000
	v_readlane_b32 s40, v251, 36
	v_readlane_b32 s41, v251, 37
	s_addc_u32 s23, s21, 0
	v_lshl_add_u64 v[80:81], v[2:3], 0, s[16:17]
	v_and_b32_e32 v2, 16, v4
	v_lshlrev_b32_e32 v206, 1, v74
	s_add_u32 s34, s20, 0x3d740000
	v_cmp_eq_u32_e64 s[40:41], 0, v2
	v_lshl_add_u64 v[2:3], s[20:21], 0, v[206:207]
	s_mov_b64 s[16:17], 0x30e78100
	v_ashrrev_i32_e32 v79, 6, v4
	s_addc_u32 s35, s21, 0
	v_and_b32_e32 v89, 15, v4
	v_lshl_add_u64 v[82:83], v[2:3], 0, s[16:17]
	v_bfe_u32 v4, v4, 1, 5
	v_lshlrev_b32_e32 v2, 5, v74
	v_mov_b32_e32 v3, v207
	v_lshlrev_b32_e32 v206, 4, v74
	v_readlane_b32 s37, v251, 33
	v_readlane_b32 s38, v251, 34
	v_readlane_b32 s39, v251, 35
	v_lshl_add_u64 v[84:85], s[14:15], 0, v[2:3]
	s_add_u32 s16, s20, 0x324f8000
	v_mul_u32_u24_e32 v86, 0x300, v4
	v_lshl_add_u64 v[4:5], s[20:21], 0, v[206:207]
	s_mov_b64 s[14:15], 0x2f5b8000
	v_lshl_add_u64 v[92:93], s[0:1], 0, v[206:207]
	v_lshl_add_u64 v[94:95], s[2:3], 0, v[2:3]
	s_mov_b64 s[0:1], 0x1000
	s_mov_b32 s12, 0
	v_cmp_gt_u32_e64 s[36:37], 48, v74
	v_lshlrev_b32_e32 v78, 2, v74
	v_cmp_lt_u32_e64 s[38:39], 31, v74
	s_addc_u32 s17, s21, 0
	v_mov_b32_e32 v87, v207
	v_and_b32_e32 v88, 8, v76
	v_lshl_add_u64 v[90:91], v[4:5], 0, s[14:15]
	v_lshl_add_u64 v[96:97], v[94:95], 0, s[0:1]
	v_readlane_b32 s27, v255, 30
	v_readlane_b32 s53, v251, 17
	v_readlane_b32 s54, v251, 18
	v_readlane_b32 s55, v251, 19
	v_readlane_b32 s58, v251, 22
	v_readlane_b32 s59, v251, 23
	v_readlane_b32 s60, v251, 24
	v_readlane_b32 s61, v251, 25
	v_readlane_b32 s64, v251, 28
	v_readlane_b32 s65, v251, 29
	v_readlane_b32 s44, v251, 40
	v_readlane_b32 s45, v251, 41
	v_readlane_b32 s46, v251, 42
	v_readlane_b32 s47, v251, 43
	v_readlane_b32 s48, v251, 44
	v_readlane_b32 s49, v251, 45
	v_readlane_b32 s50, v251, 46
	v_readlane_b32 s51, v251, 47
	v_mov_b32_e32 v184, 0
	v_mov_b32_e32 v185, 0
	v_mov_b32_e32 v186, 0
	v_mov_b32_e32 v187, 0
	v_mov_b32_e32 v188, 0
	v_mov_b32_e32 v189, 0
	v_mov_b32_e32 v190, 0
	v_mov_b32_e32 v191, 0
	s_and_saveexec_b64 s[0:1], s[36:37]
	global_load_dwordx4 v[184:187], v[84:85], off offset:16
	global_load_dwordx4 v[188:191], v[84:85], off
	s_or_b64 exec, exec, s[0:1]
	global_load_dwordx4 v[192:195], v[92:93], off
	s_mov_b32 s96, s31
	v_lshl_add_u32 v200, s96, 3, v79
	v_mov_b64_e32 v[202:203], s[22:23]
	s_movk_i32 s0, 0x1e00
	v_mad_i64_i32 v[202:203], s[2:3], v200, s0, v[202:203]
	v_mov_b32_e32 v197, v207
	v_lshlrev_b32_e32 v196, 4, v74
	v_lshl_add_u64 v[204:205], v[202:203], 0, v[196:197]
	v_mov_b32_e32 v118, 0
	v_mov_b32_e32 v119, 0
	v_mov_b32_e32 v120, 0
	v_mov_b32_e32 v121, 0
	s_and_saveexec_b64 s[0:1], s[36:37]
	global_load_dwordx4 v[118:121], v[204:205], off offset:2048
	s_or_b64 exec, exec, s[0:1]
	global_load_dwordx4 v[122:125], v[204:205], off offset:3456
	v_lshlrev_b32_e32 v196, 3, v74
	v_lshl_add_u64 v[204:205], v[202:203], 0, v[196:197]
	global_load_dwordx2 v[126:127], v[204:205], off offset:2816
	v_lshlrev_b32_e32 v196, 1, v74
	v_lshl_add_u64 v[204:205], v[202:203], 0, v[196:197]
	global_load_ushort v178, v[204:205], off offset:3328
	v_mov_b32_e32 v128, 1.0
	v_mov_b32_e32 v129, 0
	s_movk_i32 s2, 0x2000
	v_cmp_gt_i32_e64 s[0:1], s2, v200
	v_and_b32_e32 v198, 63, v200
	v_and_b32_e32 v199, 0x7ff, v200
	v_lshrrev_b32_e32 v199, 6, v199
	v_cndmask_b32_e64 v198, v199, v198, s[38:39]
	v_lshlrev_b32_e32 v199, 3, v89
	v_lshl_or_b32 v198, v198, 7, v199
	s_and_saveexec_b64 s[2:3], s[0:1]
	global_load_dwordx2 v[128:129], v198, s[34:35]
	s_or_b64 exec, exec, s[2:3]
	s_add_i32 s96, s96, s13
	s_cmp_lt_i32 s96, s24
	s_cbranch_scc0 .Lbpf_done
; template <bool MAIN, bool CONV>
; __device__ __forceinline__ void b_row(const Params& p, unsigned char* ws, int l, int row, int lane) {
;     ...
;     if (MAIN) {
;         if (lane < 48) vq = *(const u32x4*)(pr + C_CQ + lane * 8);
;         vkv = *(const u32x2*)(pr + C_CKV + lane * 4);
;         vkr = pr[C_KR + lane];
;         vs5 = *(const u32x4*)(pr + C_S5 + lane * 8);
;         if (lane < 48) { const float* g = p.in[I_QNG] + l * 384 + lane * 8; gq0 = *(const f32x4*)g; gq1 = *(const f32x4*)(g + 4); }
;         gkv = *(const f32x4*)(p.in[I_KVNG] + l * 256 + lane * 4);
;         if (lat) { const int pos = lane >= 32 ? (t & 63) : (t >> 6); rope = ((const f32x2*)(ws + WS_ROPE))[pos * 16 + (lane & 15)]; }
	v_lshl_add_u32 v200, s96, 3, v79
	v_mov_b64_e32 v[202:203], s[22:23]
	s_movk_i32 s0, 0x1e00
	v_mad_i64_i32 v[202:203], s[2:3], v200, s0, v[202:203]
	v_mov_b32_e32 v197, v207
	v_lshlrev_b32_e32 v196, 4, v74
	v_lshl_add_u64 v[204:205], v[202:203], 0, v[196:197]
	v_mov_b32_e32 v130, 0
	v_mov_b32_e32 v131, 0
	v_mov_b32_e32 v132, 0
	v_mov_b32_e32 v133, 0
	s_and_saveexec_b64 s[0:1], s[36:37]
	global_load_dwordx4 v[130:133], v[204:205], off offset:2048
	s_or_b64 exec, exec, s[0:1]
	global_load_dwordx4 v[134:137], v[204:205], off offset:3456
	v_lshlrev_b32_e32 v196, 3, v74
	v_lshl_add_u64 v[204:205], v[202:203], 0, v[196:197]
	global_load_dwordx2 v[138:139], v[204:205], off offset:2816
	v_lshlrev_b32_e32 v196, 1, v74
	v_lshl_add_u64 v[204:205], v[202:203], 0, v[196:197]
	global_load_ushort v179, v[204:205], off offset:3328
	v_mov_b32_e32 v140, 1.0
	v_mov_b32_e32 v141, 0
	s_movk_i32 s2, 0x2000
	v_cmp_gt_i32_e64 s[0:1], s2, v200
	v_and_b32_e32 v198, 63, v200
	v_and_b32_e32 v199, 0x7ff, v200
	v_lshrrev_b32_e32 v199, 6, v199
	v_cndmask_b32_e64 v198, v199, v198, s[38:39]
	v_lshlrev_b32_e32 v199, 3, v89
	v_lshl_or_b32 v198, v198, 7, v199
	s_and_saveexec_b64 s[2:3], s[0:1]
	global_load_dwordx2 v[140:141], v198, s[34:35]
	s_or_b64 exec, exec, s[2:3]
	s_add_i32 s96, s96, s13
	s_cmp_lt_i32 s96, s24
	s_cbranch_scc0 .Lbpf_done
	v_lshl_add_u32 v200, s96, 3, v79
	v_mov_b64_e32 v[202:203], s[22:23]
	s_movk_i32 s0, 0x1e00
	v_mad_i64_i32 v[202:203], s[2:3], v200, s0, v[202:203]
	v_mov_b32_e32 v197, v207
	v_lshlrev_b32_e32 v196, 4, v74
	v_lshl_add_u64 v[204:205], v[202:203], 0, v[196:197]
	v_mov_b32_e32 v142, 0
	v_mov_b32_e32 v143, 0
	v_mov_b32_e32 v144, 0
	v_mov_b32_e32 v145, 0
	s_and_saveexec_b64 s[0:1], s[36:37]
	global_load_dwordx4 v[142:145], v[204:205], off offset:2048
	s_or_b64 exec, exec, s[0:1]
	global_load_dwordx4 v[146:149], v[204:205], off offset:3456
	v_lshlrev_b32_e32 v196, 3, v74
	v_lshl_add_u64 v[204:205], v[202:203], 0, v[196:197]
	global_load_dwordx2 v[150:151], v[204:205], off offset:2816
	v_lshlrev_b32_e32 v196, 1, v74
	v_lshl_add_u64 v[204:205], v[202:203], 0, v[196:197]
	global_load_ushort v180, v[204:205], off offset:3328
	v_mov_b32_e32 v152, 1.0
	v_mov_b32_e32 v153, 0
	s_movk_i32 s2, 0x2000
	v_cmp_gt_i32_e64 s[0:1], s2, v200
	v_and_b32_e32 v198, 63, v200
	v_and_b32_e32 v199, 0x7ff, v200
	v_lshrrev_b32_e32 v199, 6, v199
	v_cndmask_b32_e64 v198, v199, v198, s[38:39]
	v_lshlrev_b32_e32 v199, 3, v89
	v_lshl_or_b32 v198, v198, 7, v199
	s_and_saveexec_b64 s[2:3], s[0:1]
	global_load_dwordx2 v[152:153], v198, s[34:35]
	s_or_b64 exec, exec, s[2:3]
	s_add_i32 s96, s96, s13
	s_cmp_lt_i32 s96, s24
	s_cbranch_scc0 .Lbpf_done
	v_lshl_add_u32 v200, s96, 3, v79
	v_mov_b64_e32 v[202:203], s[22:23]
	s_movk_i32 s0, 0x1e00
	v_mad_i64_i32 v[202:203], s[2:3], v200, s0, v[202:203]
	v_mov_b32_e32 v197, v207
	v_lshlrev_b32_e32 v196, 4, v74
	v_lshl_add_u64 v[204:205], v[202:203], 0, v[196:197]
	v_mov_b32_e32 v154, 0
	v_mov_b32_e32 v155, 0
	v_mov_b32_e32 v156, 0
	v_mov_b32_e32 v157, 0
	s_and_saveexec_b64 s[0:1], s[36:37]
	global_load_dwordx4 v[154:157], v[204:205], off offset:2048
	s_or_b64 exec, exec, s[0:1]
	global_load_dwordx4 v[158:161], v[204:205], off offset:3456
	v_lshlrev_b32_e32 v196, 3, v74
	v_lshl_add_u64 v[204:205], v[202:203], 0, v[196:197]
	global_load_dwordx2 v[162:163], v[204:205], off offset:2816
	v_lshlrev_b32_e32 v196, 1, v74
	v_lshl_add_u64 v[204:205], v[202:203], 0, v[196:197]
	global_load_ushort v181, v[204:205], off offset:3328
	v_mov_b32_e32 v164, 1.0
	v_mov_b32_e32 v165, 0
	s_movk_i32 s2, 0x2000
	v_cmp_gt_i32_e64 s[0:1], s2, v200
	v_and_b32_e32 v198, 63, v200
	v_and_b32_e32 v199, 0x7ff, v200
	v_lshrrev_b32_e32 v199, 6, v199
	v_cndmask_b32_e64 v198, v199, v198, s[38:39]
	v_lshlrev_b32_e32 v199, 3, v89
	v_lshl_or_b32 v198, v198, 7, v199
	s_and_saveexec_b64 s[2:3], s[0:1]
	global_load_dwordx2 v[164:165], v198, s[34:35]
	s_or_b64 exec, exec, s[2:3]
	s_add_i32 s96, s96, s13
	s_cmp_lt_i32 s96, s24
	s_cbranch_scc0 .Lbpf_done
	v_lshl_add_u32 v200, s96, 3, v79
	v_mov_b64_e32 v[202:203], s[22:23]
	s_movk_i32 s0, 0x1e00
	v_mad_i64_i32 v[202:203], s[2:3], v200, s0, v[202:203]
	v_mov_b32_e32 v197, v207
	v_lshlrev_b32_e32 v196, 4, v74
	v_lshl_add_u64 v[204:205], v[202:203], 0, v[196:197]
	v_mov_b32_e32 v166, 0
	v_mov_b32_e32 v167, 0
	v_mov_b32_e32 v168, 0
	v_mov_b32_e32 v169, 0
	s_and_saveexec_b64 s[0:1], s[36:37]
	global_load_dwordx4 v[166:169], v[204:205], off offset:2048
	s_or_b64 exec, exec, s[0:1]
	global_load_dwordx4 v[170:173], v[204:205], off offset:3456
	v_lshlrev_b32_e32 v196, 3, v74
	v_lshl_add_u64 v[204:205], v[202:203], 0, v[196:197]
	global_load_dwordx2 v[174:175], v[204:205], off offset:2816
	v_lshlrev_b32_e32 v196, 1, v74
	v_lshl_add_u64 v[204:205], v[202:203], 0, v[196:197]
	global_load_ushort v182, v[204:205], off offset:3328
	v_mov_b32_e32 v176, 1.0
	v_mov_b32_e32 v177, 0
	s_movk_i32 s2, 0x2000
	v_cmp_gt_i32_e64 s[0:1], s2, v200
	v_and_b32_e32 v198, 63, v200
	v_and_b32_e32 v199, 0x7ff, v200
	v_lshrrev_b32_e32 v199, 6, v199
	v_cndmask_b32_e64 v198, v199, v198, s[38:39]
	v_lshlrev_b32_e32 v199, 3, v89
	v_lshl_or_b32 v198, v198, 7, v199
	s_and_saveexec_b64 s[2:3], s[0:1]
	global_load_dwordx2 v[176:177], v198, s[34:35]
	s_or_b64 exec, exec, s[2:3]
.Lbpf_done:
	s_waitcnt vmcnt(0)
	s_branch .LBB0_469

; __device__ __forceinline__ float bflo(unsigned w) { return __uint_as_float(w << 16); }
; __device__ __forceinline__ float bfhi(unsigned w) { return __uint_as_float(w & 0xffff0000u); }
; template <bool MAIN, bool CONV>
; __device__ __forceinline__ void b_row(const Params& p, unsigned char* ws, int l, int row, int lane) {
;     ...
;     if (MAIN) {
;         if (lane < 48) vq = *(const u32x4*)(pr + C_CQ + lane * 8);
;         vkv = *(const u32x2*)(pr + C_CKV + lane * 4);
;         vkr = pr[C_KR + lane];
;         vs5 = *(const u32x4*)(pr + C_S5 + lane * 8);
;         if (lane < 48) { const float* g = p.in[I_QNG] + l * 384 + lane * 8; gq0 = *(const f32x4*)g; gq1 = *(const f32x4*)(g + 4); }
;         gkv = *(const f32x4*)(p.in[I_KVNG] + l * 256 + lane * 4);
;         if (lat) { const int pos = lane >= 32 ? (t & 63) : (t >> 6); rope = ((const f32x2*)(ws + WS_ROPE))[pos * 16 + (lane & 15)]; }
;     }
;     if (CONV) {
;         ca = *(const u32x4*)(pr + C_CVC + c0); ch = *(const u32x4*)(pr + C_CVH + c0); bg = *(const u32x4*)(pr + C_CVB + c0);
;         if (t > 0) { pa = *(const u32x4*)(pr - INP + C_CVC + c0); ph = *(const u32x4*)(pr - INP + C_CVH + c0); }
;         if (t < seqlen - 1) { na = *(const u32x4*)(pr + INP + C_CVC + c0); nh = *(const u32x4*)(pr + INP + C_CVH + c0); }
;         const float* cw = p.in[I_CONVW] + (size_t)l * 3 * 512 + c0;
;         cw0a = *(const f32x4*)cw; cw0b = *(const f32x4*)(cw + 4); cw1a = *(const f32x4*)(cw + 512); cw1b = *(const f32x4*)(cw + 516); cw2a = *(const f32x4*)(cw + 1024); cw2b = *(const f32x4*)(cw + 1028);
;     }
;     asm volatile("" ::: "memory");
;     if (MAIN) {
;         { float f[8]; float ss = 0.f;
;           if (lane < 48) { const u32x4 v = vq; f[0] = bflo(v.x); f[1] = bfhi(v.x); f[2] = bflo(v.y); f[3] = bfhi(v.y); f[4] = bflo(v.z); f[5] = bfhi(v.z); f[6] = bflo(v.w); f[7] = bfhi(v.w);
;     #pragma unroll
;               for (int j = 0; j < 8; ++j) ss += f[j] * f[j]; }
.LBB0_528:
	s_and_b64 vcc, exec, s[0:1]
	s_cbranch_vccz .LBB0_468
	v_mov_b32_e32 v18, v118
	v_mov_b32_e32 v19, v119
	v_mov_b32_e32 v20, v120
	v_mov_b32_e32 v21, v121
	v_mov_b32_e32 v2, v122
	v_mov_b32_e32 v3, v123
	v_mov_b32_e32 v4, v124
	v_mov_b32_e32 v5, v125
	v_mov_b32_e32 v24, v126
	v_mov_b32_e32 v25, v127
	v_mov_b32_e32 v22, v128
	v_mov_b32_e32 v23, v129
	v_mov_b32_e32 v34, v178
	v_mov_b32_e32 v6, v184
	v_mov_b32_e32 v7, v185
	v_mov_b32_e32 v8, v186
	v_mov_b32_e32 v9, v187
	v_mov_b32_e32 v14, v188
	v_mov_b32_e32 v15, v189
	v_mov_b32_e32 v16, v190
	v_mov_b32_e32 v17, v191
	v_mov_b32_e32 v10, v192
	v_mov_b32_e32 v11, v193
	v_mov_b32_e32 v12, v194
	v_mov_b32_e32 v13, v195
	v_mov_b32_e32 v35, 0
	v_mov_b32_e32 v118, v130
	v_mov_b32_e32 v119, v131
	v_mov_b32_e32 v120, v132
	v_mov_b32_e32 v121, v133
	v_mov_b32_e32 v122, v134
	v_mov_b32_e32 v123, v135
	v_mov_b32_e32 v124, v136
	v_mov_b32_e32 v125, v137
	v_mov_b32_e32 v126, v138
	v_mov_b32_e32 v127, v139
	v_mov_b32_e32 v128, v140
	v_mov_b32_e32 v129, v141
	v_mov_b32_e32 v178, v179
	v_mov_b32_e32 v130, v142
	v_mov_b32_e32 v131, v143
	v_mov_b32_e32 v132, v144
	v_mov_b32_e32 v133, v145
	v_mov_b32_e32 v134, v146
	v_mov_b32_e32 v135, v147
	v_mov_b32_e32 v136, v148
	v_mov_b32_e32 v137, v149
	v_mov_b32_e32 v138, v150
	v_mov_b32_e32 v139, v151
	v_mov_b32_e32 v140, v152
	v_mov_b32_e32 v141, v153
	v_mov_b32_e32 v179, v180
	v_mov_b32_e32 v142, v154
	v_mov_b32_e32 v143, v155
	v_mov_b32_e32 v144, v156
	v_mov_b32_e32 v145, v157
	v_mov_b32_e32 v146, v158
	v_mov_b32_e32 v147, v159
	v_mov_b32_e32 v148, v160
	v_mov_b32_e32 v149, v161
	v_mov_b32_e32 v150, v162
	v_mov_b32_e32 v151, v163
	v_mov_b32_e32 v152, v164
	v_mov_b32_e32 v153, v165
	v_mov_b32_e32 v180, v181
	v_mov_b32_e32 v154, v166
	v_mov_b32_e32 v155, v167
	v_mov_b32_e32 v156, v168
	v_mov_b32_e32 v157, v169
	v_mov_b32_e32 v158, v170
	v_mov_b32_e32 v159, v171
	v_mov_b32_e32 v160, v172
	v_mov_b32_e32 v161, v173
	v_mov_b32_e32 v162, v174
	v_mov_b32_e32 v163, v175
	v_mov_b32_e32 v164, v176
	v_mov_b32_e32 v165, v177
	v_mov_b32_e32 v181, v182
	v_mov_b32_e32 v26, 0
	v_mov_b32_e32 v27, 0
	v_mov_b32_e32 v28, 0
	v_mov_b32_e32 v29, 0
	v_mov_b32_e32 v30, 0
	v_mov_b32_e32 v31, 0
	v_mov_b32_e32 v32, 0
	v_mov_b32_e32 v33, 0
	s_and_saveexec_b64 s[0:1], s[36:37]
	s_cbranch_execz .LBB0_537
	v_lshlrev_b32_e32 v26, 16, v18
	v_and_b32_e32 v27, 0xffff0000, v18
	v_pk_mul_f32 v[36:37], v[26:27], v[26:27]
	v_and_b32_e32 v18, 0xffff0000, v19
	v_lshlrev_b32_e32 v19, 16, v19
	v_pk_mov_b32 v[28:29], v[18:19], v[18:19] op_sel:[1,0]
	v_pk_mul_f32 v[18:19], v[18:19], v[18:19]
	v_add_f32_e32 v35, v36, v37
	v_and_b32_e32 v32, 0xffff0000, v20
	v_lshlrev_b32_e32 v33, 16, v20
	v_add_f32_e32 v19, v19, v35
	v_pk_mul_f32 v[38:39], v[32:33], v[32:33]
	v_add_f32_e32 v18, v18, v19
	v_and_b32_e32 v20, 0xffff0000, v21
	v_lshlrev_b32_e32 v21, 16, v21
	v_add_f32_e32 v18, v39, v18
	v_pk_mov_b32 v[30:31], v[32:33], v[32:33] op_sel:[1,0]
	v_pk_mov_b32 v[32:33], v[20:21], v[20:21] op_sel:[1,0]
	v_pk_mul_f32 v[20:21], v[20:21], v[20:21]
	v_add_f32_e32 v18, v38, v18
	v_add_f32_e32 v18, v21, v18
	v_add_f32_e32 v35, v20, v18
